# attention sub-tiles: the no-rescale branch targets (start of the exponentials) aligned to 64 bytes
# speedup vs baseline: 1.0003x; 1.0003x over previous
.LBB0_452:
	s_nop 0
	v_max3_f32 v2, v70, v71, v72
	v_max3_f32 v4, v73, v74, v75
	v_max3_f32 v5, v76, v77, v78
	v_max3_f32 v175, v79, v80, v81
	v_max3_f32 v2, v2, v4, v5
	v_max3_f32 v4, v82, v83, v84
	v_max3_f32 v2, v2, v175, v4
	v_max_f32_e32 v2, v2, v85
	v_sub_f32_e32 v4, v2, v168
	v_cmp_ge_f32_e32 vcc, s76, v4
	s_cmp_eq_u64 vcc, exec
	s_cbranch_scc1 .LBB0_454
	v_mov_b32_e32 v4, v2
	s_nop 1
	v_permlane32_swap_b32_e32 v2, v4
	v_max_f32_e32 v2, v2, v4
	v_max_f32_e32 v2, v2, v2
	v_max_f32_e32 v4, v168, v168
	v_max_f32_e32 v4, v4, v2
	v_sub_f32_e32 v2, v168, v4
	v_mul_f32_e32 v2, 0x3fb8aa3b, v2
	v_exp_f32_e32 v2, v2
	v_mov_b32_e32 v168, v4
	v_mul_f32_e32 v167, v167, v2
	v_pk_mul_f32 v[68:69], v[68:69], v[2:3] op_sel_hi:[1,0]
	v_pk_mul_f32 v[66:67], v[66:67], v[2:3] op_sel_hi:[1,0]
	v_pk_mul_f32 v[64:65], v[64:65], v[2:3] op_sel_hi:[1,0]
	v_pk_mul_f32 v[62:63], v[62:63], v[2:3] op_sel_hi:[1,0]
	v_pk_mul_f32 v[60:61], v[60:61], v[2:3] op_sel_hi:[1,0]
	v_pk_mul_f32 v[58:59], v[58:59], v[2:3] op_sel_hi:[1,0]
	v_pk_mul_f32 v[56:57], v[56:57], v[2:3] op_sel_hi:[1,0]
	v_pk_mul_f32 v[54:55], v[54:55], v[2:3] op_sel_hi:[1,0]
	v_pk_mul_f32 v[52:53], v[52:53], v[2:3] op_sel_hi:[1,0]
	v_pk_mul_f32 v[50:51], v[50:51], v[2:3] op_sel_hi:[1,0]
	v_pk_mul_f32 v[48:49], v[48:49], v[2:3] op_sel_hi:[1,0]
	v_pk_mul_f32 v[46:47], v[46:47], v[2:3] op_sel_hi:[1,0]
	v_pk_mul_f32 v[44:45], v[44:45], v[2:3] op_sel_hi:[1,0]
	v_pk_mul_f32 v[42:43], v[42:43], v[2:3] op_sel_hi:[1,0]
	v_pk_mul_f32 v[40:41], v[40:41], v[2:3] op_sel_hi:[1,0]
	v_pk_mul_f32 v[38:39], v[38:39], v[2:3] op_sel_hi:[1,0]
	v_pk_mul_f32 v[36:37], v[36:37], v[2:3] op_sel_hi:[1,0]
	v_pk_mul_f32 v[34:35], v[34:35], v[2:3] op_sel_hi:[1,0]
	v_pk_mul_f32 v[32:33], v[32:33], v[2:3] op_sel_hi:[1,0]
	v_pk_mul_f32 v[30:31], v[30:31], v[2:3] op_sel_hi:[1,0]
	v_pk_mul_f32 v[28:29], v[28:29], v[2:3] op_sel_hi:[1,0]
	v_pk_mul_f32 v[26:27], v[26:27], v[2:3] op_sel_hi:[1,0]
	v_pk_mul_f32 v[24:25], v[24:25], v[2:3] op_sel_hi:[1,0]
	v_pk_mul_f32 v[22:23], v[22:23], v[2:3] op_sel_hi:[1,0]
	v_pk_mul_f32 v[20:21], v[20:21], v[2:3] op_sel_hi:[1,0]
	v_pk_mul_f32 v[18:19], v[18:19], v[2:3] op_sel_hi:[1,0]
	v_pk_mul_f32 v[16:17], v[16:17], v[2:3] op_sel_hi:[1,0]
	v_pk_mul_f32 v[14:15], v[14:15], v[2:3] op_sel_hi:[1,0]
	v_pk_mul_f32 v[12:13], v[12:13], v[2:3] op_sel_hi:[1,0]
	v_pk_mul_f32 v[10:11], v[10:11], v[2:3] op_sel_hi:[1,0]
	v_pk_mul_f32 v[8:9], v[8:9], v[2:3] op_sel_hi:[1,0]
	v_pk_mul_f32 v[6:7], v[6:7], v[2:3] op_sel_hi:[1,0]
	.p2align 6

.LBB0_458:
	s_nop 0
	v_max3_f32 v2, v70, v71, v72
	v_max3_f32 v4, v73, v74, v75
	v_max3_f32 v5, v76, v77, v78
	v_max3_f32 v169, v79, v80, v81
	v_max3_f32 v2, v2, v4, v5
	v_max3_f32 v4, v82, v83, v84
	v_max3_f32 v2, v2, v169, v4
	v_max_f32_e32 v2, v2, v85
	v_sub_f32_e32 v4, v2, v168
	v_cmp_ge_f32_e32 vcc, s76, v4
	s_cmp_eq_u64 vcc, exec
	s_cbranch_scc1 .LBB0_460
	v_mov_b32_e32 v4, v2
	s_nop 1
	v_permlane32_swap_b32_e32 v2, v4
	v_max_f32_e32 v2, v2, v4
	v_max_f32_e32 v2, v2, v2
	v_max_f32_e32 v4, v168, v168
	v_max_f32_e32 v4, v4, v2
	v_sub_f32_e32 v2, v168, v4
	v_mul_f32_e32 v2, 0x3fb8aa3b, v2
	v_exp_f32_e32 v2, v2
	v_mov_b32_e32 v168, v4
	v_mul_f32_e32 v167, v167, v2
	v_pk_mul_f32 v[68:69], v[68:69], v[2:3] op_sel_hi:[1,0]
	v_pk_mul_f32 v[66:67], v[66:67], v[2:3] op_sel_hi:[1,0]
	v_pk_mul_f32 v[64:65], v[64:65], v[2:3] op_sel_hi:[1,0]
	v_pk_mul_f32 v[62:63], v[62:63], v[2:3] op_sel_hi:[1,0]
	v_pk_mul_f32 v[60:61], v[60:61], v[2:3] op_sel_hi:[1,0]
	v_pk_mul_f32 v[58:59], v[58:59], v[2:3] op_sel_hi:[1,0]
	v_pk_mul_f32 v[56:57], v[56:57], v[2:3] op_sel_hi:[1,0]
	v_pk_mul_f32 v[54:55], v[54:55], v[2:3] op_sel_hi:[1,0]
	v_pk_mul_f32 v[52:53], v[52:53], v[2:3] op_sel_hi:[1,0]
	v_pk_mul_f32 v[50:51], v[50:51], v[2:3] op_sel_hi:[1,0]
	v_pk_mul_f32 v[48:49], v[48:49], v[2:3] op_sel_hi:[1,0]
	v_pk_mul_f32 v[46:47], v[46:47], v[2:3] op_sel_hi:[1,0]
	v_pk_mul_f32 v[44:45], v[44:45], v[2:3] op_sel_hi:[1,0]
	v_pk_mul_f32 v[42:43], v[42:43], v[2:3] op_sel_hi:[1,0]
	v_pk_mul_f32 v[40:41], v[40:41], v[2:3] op_sel_hi:[1,0]
	v_pk_mul_f32 v[38:39], v[38:39], v[2:3] op_sel_hi:[1,0]
	v_pk_mul_f32 v[36:37], v[36:37], v[2:3] op_sel_hi:[1,0]
	v_pk_mul_f32 v[34:35], v[34:35], v[2:3] op_sel_hi:[1,0]
	v_pk_mul_f32 v[32:33], v[32:33], v[2:3] op_sel_hi:[1,0]
	v_pk_mul_f32 v[30:31], v[30:31], v[2:3] op_sel_hi:[1,0]
	v_pk_mul_f32 v[28:29], v[28:29], v[2:3] op_sel_hi:[1,0]
	v_pk_mul_f32 v[26:27], v[26:27], v[2:3] op_sel_hi:[1,0]
	v_pk_mul_f32 v[24:25], v[24:25], v[2:3] op_sel_hi:[1,0]
	v_pk_mul_f32 v[22:23], v[22:23], v[2:3] op_sel_hi:[1,0]
	v_pk_mul_f32 v[20:21], v[20:21], v[2:3] op_sel_hi:[1,0]
	v_pk_mul_f32 v[18:19], v[18:19], v[2:3] op_sel_hi:[1,0]
	v_pk_mul_f32 v[16:17], v[16:17], v[2:3] op_sel_hi:[1,0]
	v_pk_mul_f32 v[14:15], v[14:15], v[2:3] op_sel_hi:[1,0]
	v_pk_mul_f32 v[12:13], v[12:13], v[2:3] op_sel_hi:[1,0]
	v_pk_mul_f32 v[10:11], v[10:11], v[2:3] op_sel_hi:[1,0]
	v_pk_mul_f32 v[8:9], v[8:9], v[2:3] op_sel_hi:[1,0]
	v_pk_mul_f32 v[6:7], v[6:7], v[2:3] op_sel_hi:[1,0]
	.p2align 6

.Lpf_win_skip:
	s_cmp_lt_i32 s17, 0
	.p2align 8
	s_cbranch_scc1 .LBB0_532
	s_add_i32 s22, s18, 1
	v_and_b32_e32 v2, 63, v4
	v_cvt_f32_ubyte0_e32 v4, s22
	s_mov_b32 s22, 0x42fc0000
	v_cmp_lt_f32_e32 vcc, s22, v4
	v_mov_b32_e32 v5, 0x42800000
	s_and_b64 s[24:25], vcc, exec
	v_cndmask_b32_e32 v5, 0, v5, vcc
	v_sub_f32_e32 v4, v5, v4
	v_exp_f32_e32 v4, v4
	s_cselect_b32 s23, 0xffffffc0, 0
	v_bfe_u32 v6, v2, 1, 4
	v_cmp_gt_u32_e64 s[36:37], 32, v2
	v_ldexp_f32 v4, v4, s23
	v_mul_f32_e32 v5, 0x43800000, v4
	v_and_b32_e32 v4, 0x7fff0000, v4
	v_or_b32_sdwa v4, v5, v4 dst_sel:DWORD dst_unused:UNUSED_PAD src0_sel:WORD_1 src1_sel:DWORD
	v_lshlrev_b32_e32 v5, 7, v2
	v_and_b32_e32 v100, 0xf00, v5
	v_lshlrev_b32_e32 v5, 3, v2
	v_and_b32_e32 v94, 8, v5
	v_or_b32_e32 v5, v94, v98
	v_bitop3_b32 v7, v94, v6, v98 bitop3:0x36
	v_lshlrev_b32_e32 v101, 4, v7
	v_bitop3_b32 v7, v5, v6, 2 bitop3:0x36
	v_lshlrev_b32_e32 v102, 4, v7
	v_bitop3_b32 v7, v5, v6, 4 bitop3:0x36
	v_bitop3_b32 v5, v5, v6, 6 bitop3:0x36
	v_lshlrev_b32_e32 v104, 4, v5
	v_lshrrev_b32_e32 v5, 2, v2
	v_lshlrev_b32_e32 v103, 4, v7
	v_and_b32_e32 v5, 2, v5
	v_lshrrev_b32_e32 v6, 3, v2
	v_bfe_u32 v7, v2, 1, 1
	v_cndmask_b32_e64 v82, 0, v4, s[36:37]
	v_lshrrev_b32_e32 v4, 1, v2
	v_and_or_b32 v5, v6, 4, v5
	v_and_or_b32 v6, v6, 2, v7
	v_bfe_u32 v2, v2, 3, 1
	v_and_or_b32 v2, v4, 2, v2
	v_lshlrev_b32_e32 v4, 4, v6
	v_lshl_or_b32 v2, v2, 6, v4
	v_lshlrev_b32_e32 v4, 2, v98
	v_lshlrev_b32_e32 v5, 7, v5
	v_or_b32_e32 v105, v2, v5
	v_bitop3_b32 v106, v2, 64, v5 bitop3:0x36
	v_sub_u32_e32 v2, v4, v99
	v_mov_b32_e32 v16, v3
	v_mov_b32_e32 v17, v3
	s_add_i32 s26, s2, s3
	s_sub_i32 s27, 0, s2
	s_lshl_b32 s2, s2, 6
	v_sub_u32_e32 v108, v99, v4
	v_subrev_u32_e32 v109, s19, v2
	v_mov_b32_e32 v2, v3
	v_mov_b32_e32 v4, v3
	v_mov_b32_e32 v5, v3
	v_mov_b32_e32 v6, v3
	v_mov_b32_e32 v7, v3
	v_mov_b32_e32 v8, v3
	v_mov_b32_e32 v9, v3
	v_mov_b32_e32 v10, v3
	v_mov_b32_e32 v11, v3
	v_mov_b32_e32 v12, v3
	v_mov_b32_e32 v13, v3
	v_mov_b32_e32 v14, v3
	v_mov_b32_e32 v15, v3
	v_mov_b64_e32 v[32:33], v[16:17]
	v_mov_b64_e32 v[48:49], v[16:17]
	s_mov_b32 s21, 32
	s_mov_b32 s22, 0
	v_mov_b32_e32 v83, v3
	v_mov_b32_e32 v84, v3
	v_mov_b32_e32 v85, v3
	s_or_b32 s23, s20, 31
	s_add_i32 s24, s20, 0xfffffe01
	s_mov_b32 s25, 3
	s_sub_i32 s26, 0, s26
	s_sub_i32 s28, s27, s3
	s_sub_i32 s29, 0, s2
	v_mov_b32_e32 v110, 0xf149f2ca
	v_mov_b32_e32 v107, 0
	s_mov_b32 s30, 0
	v_mov_b64_e32 v[30:31], v[14:15]
	v_mov_b64_e32 v[28:29], v[12:13]
	v_mov_b64_e32 v[26:27], v[10:11]
	v_mov_b64_e32 v[24:25], v[8:9]
	v_mov_b64_e32 v[22:23], v[6:7]
	v_mov_b64_e32 v[20:21], v[4:5]
	v_mov_b64_e32 v[18:19], v[2:3]
	v_mov_b64_e32 v[46:47], v[14:15]
	v_mov_b64_e32 v[44:45], v[12:13]
	v_mov_b64_e32 v[42:43], v[10:11]
	v_mov_b64_e32 v[40:41], v[8:9]
	v_mov_b64_e32 v[38:39], v[6:7]
	v_mov_b64_e32 v[36:37], v[4:5]
	v_mov_b64_e32 v[34:35], v[2:3]
	s_branch .LBB0_511
	.p2align 6

.LBB0_524:
	s_nop 1
	v_max3_f32 v2, v50, v51, v52
	v_max3_f32 v116, v53, v54, v55
	v_max3_f32 v117, v56, v57, v58
	v_max3_f32 v118, v59, v60, v61
	v_max3_f32 v2, v2, v116, v117
	v_max3_f32 v116, v62, v63, v64
	v_max3_f32 v2, v2, v118, v116
	v_max_f32_e32 v2, v2, v65
	v_sub_f32_e32 v116, v2, v110
	v_cmp_ge_f32_e32 vcc, s76, v116
	s_cmp_eq_u64 vcc, exec
	s_cbranch_scc1 .LBB0_526
	v_mov_b32_e32 v116, v2
	s_nop 1
	v_permlane32_swap_b32_e32 v2, v116
	v_max_f32_e32 v2, v2, v116
	v_max_f32_e32 v2, v2, v2
	v_max_f32_e32 v116, v110, v110
	v_max_f32_e32 v116, v116, v2
	v_sub_f32_e32 v2, v110, v116
	v_mul_f32_e32 v2, 0x3fb8aa3b, v2
	v_exp_f32_e32 v2, v2
	v_mov_b32_e32 v110, v116
	v_mul_f32_e32 v107, v107, v2
	v_pk_mul_f32 v[48:49], v[48:49], v[2:3] op_sel_hi:[1,0]
	v_pk_mul_f32 v[46:47], v[46:47], v[2:3] op_sel_hi:[1,0]
	v_pk_mul_f32 v[44:45], v[44:45], v[2:3] op_sel_hi:[1,0]
	v_pk_mul_f32 v[42:43], v[42:43], v[2:3] op_sel_hi:[1,0]
	v_pk_mul_f32 v[40:41], v[40:41], v[2:3] op_sel_hi:[1,0]
	v_pk_mul_f32 v[38:39], v[38:39], v[2:3] op_sel_hi:[1,0]
	v_pk_mul_f32 v[36:37], v[36:37], v[2:3] op_sel_hi:[1,0]
	v_pk_mul_f32 v[34:35], v[34:35], v[2:3] op_sel_hi:[1,0]
	v_pk_mul_f32 v[32:33], v[32:33], v[2:3] op_sel_hi:[1,0]
	v_pk_mul_f32 v[30:31], v[30:31], v[2:3] op_sel_hi:[1,0]
	v_pk_mul_f32 v[28:29], v[28:29], v[2:3] op_sel_hi:[1,0]
	v_pk_mul_f32 v[26:27], v[26:27], v[2:3] op_sel_hi:[1,0]
	v_pk_mul_f32 v[24:25], v[24:25], v[2:3] op_sel_hi:[1,0]
	v_pk_mul_f32 v[22:23], v[22:23], v[2:3] op_sel_hi:[1,0]
	v_pk_mul_f32 v[20:21], v[20:21], v[2:3] op_sel_hi:[1,0]
	v_pk_mul_f32 v[18:19], v[18:19], v[2:3] op_sel_hi:[1,0]
	.p2align 6

.LBB0_666:
	s_cmp_eq_u32 s2, 0
	.p2align 8
	s_cbranch_scc1 .LBB0_697
	s_add_i32 s0, s15, 1
	v_cvt_f32_ubyte0_e32 v2, s0
	s_mov_b32 s0, 0x42fc0000
	v_cmp_lt_f32_e32 vcc, s0, v2
	v_mov_b32_e32 v11, 0x42800000
	s_and_b64 s[0:1], vcc, exec
	v_cndmask_b32_e32 v11, 0, v11, vcc
	v_sub_f32_e32 v2, v11, v2
	v_exp_f32_e32 v2, v2
	s_cselect_b32 s0, 0xffffffc0, 0
	v_mov_b32_e32 v16, v3
	v_mov_b32_e32 v17, v3
	v_ldexp_f32 v2, v2, s0
	v_mul_f32_e32 v11, 0x43800000, v2
	v_and_b32_e32 v2, 0x7fff0000, v2
	v_or_b32_sdwa v2, v11, v2 dst_sel:DWORD dst_unused:UNUSED_PAD src0_sel:WORD_1 src1_sel:DWORD
	v_cndmask_b32_e64 v114, 0, v2, s[22:23]
	v_bitop3_b32 v2, v67, v6, 15 bitop3:0x78
	v_lshlrev_b32_e32 v137, 4, v2
	v_bitop3_b32 v2, v10, v6, 15 bitop3:0x78
	v_lshlrev_b32_e32 v138, 4, v2
	v_bitop3_b32 v2, v9, v6, 15 bitop3:0x78
	v_lshlrev_b32_e32 v139, 4, v2
	v_bitop3_b32 v2, v8, v6, 15 bitop3:0x78
	v_lshlrev_b32_e32 v140, 4, v2
	v_and_or_b32 v2, v6, 1, v5
	v_lshl_or_b32 v2, v2, 4, v7
	v_or_b32_e32 v156, v2, v4
	v_bitop3_b32 v157, v2, 64, v4 bitop3:0x36
	v_mov_b32_e32 v2, v3
	v_mov_b32_e32 v4, v3
	v_mov_b32_e32 v5, v3
	v_mov_b32_e32 v6, v3
	v_mov_b32_e32 v7, v3
	v_mov_b32_e32 v8, v3
	v_mov_b32_e32 v9, v3
	v_mov_b32_e32 v10, v3
	v_mov_b32_e32 v11, v3
	v_mov_b32_e32 v12, v3
	v_mov_b32_e32 v13, v3
	v_mov_b32_e32 v14, v3
	v_mov_b32_e32 v15, v3
	v_mov_b64_e32 v[80:81], v[16:17]
	v_mov_b64_e32 v[64:65], v[16:17]
	s_mov_b32 s5, 0
	v_mov_b32_e32 v115, v3
	v_mov_b32_e32 v116, v3
	v_mov_b32_e32 v117, v3
	s_or_b32 s6, s16, 31
	v_add_u32_e32 v141, -2, v126
	v_add_u32_e32 v142, -3, v126
	v_add_u32_e32 v143, -8, v126
	v_add_u32_e32 v145, -9, v126
	v_add_u32_e32 v146, -10, v126
	v_add_u32_e32 v147, -11, v126
	v_add_u32_e32 v148, -16, v126
	v_subrev_u32_e32 v149, 17, v126
	v_subrev_u32_e32 v150, 18, v126
	v_subrev_u32_e32 v151, 19, v126
	v_subrev_u32_e32 v152, 24, v126
	v_subrev_u32_e32 v153, 25, v126
	v_subrev_u32_e32 v154, 26, v126
	v_subrev_u32_e32 v155, 27, v126
	v_mov_b32_e32 v144, 0
	v_mov_b32_e32 v158, 0xf149f2ca
	s_mov_b32 s7, -1
	v_mov_b64_e32 v[78:79], v[14:15]
	v_mov_b64_e32 v[76:77], v[12:13]
	v_mov_b64_e32 v[74:75], v[10:11]
	v_mov_b64_e32 v[72:73], v[8:9]
	v_mov_b64_e32 v[70:71], v[6:7]
	v_mov_b64_e32 v[68:69], v[4:5]
	v_mov_b64_e32 v[66:67], v[2:3]
	v_mov_b64_e32 v[62:63], v[14:15]
	v_mov_b64_e32 v[60:61], v[12:13]
	v_mov_b64_e32 v[58:59], v[10:11]
	v_mov_b64_e32 v[56:57], v[8:9]
	v_mov_b64_e32 v[54:55], v[6:7]
	v_mov_b64_e32 v[52:53], v[4:5]
	v_mov_b64_e32 v[50:51], v[2:3]
	s_branch .LBB0_670
	.p2align 6

.LBB0_687:
	s_nop 0
	v_max3_f32 v2, v82, v83, v84
	v_max3_f32 v164, v85, v86, v87
	v_max3_f32 v165, v88, v89, v90
	v_max3_f32 v166, v91, v92, v93
	v_max3_f32 v2, v2, v164, v165
	v_max3_f32 v164, v94, v95, v96
	v_max3_f32 v2, v2, v166, v164
	v_max_f32_e32 v2, v2, v97
	v_sub_f32_e32 v164, v2, v158
	v_cmp_ge_f32_e32 vcc, s76, v164
	s_cmp_eq_u64 vcc, exec
	s_cbranch_scc1 .LBB0_689
	v_mov_b32_e32 v164, v2
	s_nop 1
	v_permlane32_swap_b32_e32 v2, v164
	v_max_f32_e32 v2, v2, v164
	v_max_f32_e32 v2, v2, v2
	v_max_f32_e32 v164, v158, v158
	v_max_f32_e32 v164, v164, v2
	v_sub_f32_e32 v2, v158, v164
	v_mul_f32_e32 v2, 0x3fb8aa3b, v2
	v_exp_f32_e32 v2, v2
	v_mov_b32_e32 v158, v164
	v_mul_f32_e32 v144, v144, v2
	v_pk_mul_f32 v[80:81], v[80:81], v[2:3] op_sel_hi:[1,0]
	v_pk_mul_f32 v[78:79], v[78:79], v[2:3] op_sel_hi:[1,0]
	v_pk_mul_f32 v[76:77], v[76:77], v[2:3] op_sel_hi:[1,0]
	v_pk_mul_f32 v[74:75], v[74:75], v[2:3] op_sel_hi:[1,0]
	v_pk_mul_f32 v[72:73], v[72:73], v[2:3] op_sel_hi:[1,0]
	v_pk_mul_f32 v[70:71], v[70:71], v[2:3] op_sel_hi:[1,0]
	v_pk_mul_f32 v[68:69], v[68:69], v[2:3] op_sel_hi:[1,0]
	v_pk_mul_f32 v[66:67], v[66:67], v[2:3] op_sel_hi:[1,0]
	v_pk_mul_f32 v[64:65], v[64:65], v[2:3] op_sel_hi:[1,0]
	v_pk_mul_f32 v[62:63], v[62:63], v[2:3] op_sel_hi:[1,0]
	v_pk_mul_f32 v[60:61], v[60:61], v[2:3] op_sel_hi:[1,0]
	v_pk_mul_f32 v[58:59], v[58:59], v[2:3] op_sel_hi:[1,0]
	v_pk_mul_f32 v[56:57], v[56:57], v[2:3] op_sel_hi:[1,0]
	v_pk_mul_f32 v[54:55], v[54:55], v[2:3] op_sel_hi:[1,0]
	v_pk_mul_f32 v[52:53], v[52:53], v[2:3] op_sel_hi:[1,0]
	v_pk_mul_f32 v[50:51], v[50:51], v[2:3] op_sel_hi:[1,0]
	.p2align 6

.Lpf_swa_skip:
	s_cmp_lt_i32 s13, 0
	.p2align 8
	s_cbranch_scc1 .LBB0_793
	v_and_b32_e32 v2, 63, v4
	v_mul_f32_e32 v4, 0x43800000, v100
	v_and_b32_e32 v5, 0x7fff0000, v100
	v_or_b32_sdwa v4, v4, v5 dst_sel:DWORD dst_unused:UNUSED_PAD src0_sel:WORD_1 src1_sel:DWORD
	v_lshlrev_b32_e32 v5, 7, v2
	v_and_b32_e32 v103, 0xf00, v5
	v_lshlrev_b32_e32 v5, 3, v2
	v_and_b32_e32 v96, 8, v5
	v_bfe_u32 v6, v2, 1, 4
	v_or_b32_e32 v5, v96, v101
	v_bitop3_b32 v7, v96, v6, v101 bitop3:0x36
	v_lshlrev_b32_e32 v104, 4, v7
	v_bitop3_b32 v7, v5, v6, 2 bitop3:0x36
	v_lshlrev_b32_e32 v105, 4, v7
	v_bitop3_b32 v7, v5, v6, 4 bitop3:0x36
	v_bitop3_b32 v5, v5, v6, 6 bitop3:0x36
	v_lshlrev_b32_e32 v107, 4, v5
	v_lshrrev_b32_e32 v5, 2, v2
	v_cmp_gt_u32_e64 s[36:37], 32, v2
	v_lshlrev_b32_e32 v106, 4, v7
	v_and_b32_e32 v5, 2, v5
	v_lshrrev_b32_e32 v6, 3, v2
	v_bfe_u32 v7, v2, 1, 1
	v_cndmask_b32_e64 v82, 0, v4, s[36:37]
	v_lshrrev_b32_e32 v4, 1, v2
	v_and_or_b32 v5, v6, 4, v5
	v_and_or_b32 v6, v6, 2, v7
	v_bfe_u32 v2, v2, 3, 1
	v_and_or_b32 v2, v4, 2, v2
	v_lshlrev_b32_e32 v4, 4, v6
	v_lshl_or_b32 v2, v2, 6, v4
	v_lshlrev_b32_e32 v4, 2, v101
	v_lshlrev_b32_e32 v5, 7, v5
	v_or_b32_e32 v109, v2, v5
	v_bitop3_b32 v110, v2, 64, v5 bitop3:0x36
	v_sub_u32_e32 v2, v4, v102
	v_mov_b32_e32 v16, v3
	v_mov_b32_e32 v17, v3
	s_add_i32 s22, s0, s1
	s_sub_i32 s23, 0, s0
	s_lshl_b32 s0, s0, 6
	v_sub_u32_e32 v111, v102, v4
	v_subrev_u32_e32 v112, s15, v2
	v_mov_b32_e32 v2, v3
	v_mov_b32_e32 v4, v3
	v_mov_b32_e32 v5, v3
	v_mov_b32_e32 v6, v3
	v_mov_b32_e32 v7, v3
	v_mov_b32_e32 v8, v3
	v_mov_b32_e32 v9, v3
	v_mov_b32_e32 v10, v3
	v_mov_b32_e32 v11, v3
	v_mov_b32_e32 v12, v3
	v_mov_b32_e32 v13, v3
	v_mov_b32_e32 v14, v3
	v_mov_b32_e32 v15, v3
	v_mov_b64_e32 v[32:33], v[16:17]
	v_mov_b64_e32 v[48:49], v[16:17]
	s_mov_b32 s18, 32
	v_mov_b32_e32 v83, v3
	v_mov_b32_e32 v84, v3
	v_mov_b32_e32 v85, v3
	s_or_b32 s19, s16, 31
	s_add_i32 s20, s16, 0xffffff81
	s_mov_b32 s21, 3
	s_sub_i32 s22, 0, s22
	s_sub_i32 s24, s23, s1
	s_sub_i32 s25, 0, s0
	v_mov_b32_e32 v113, 0xf149f2ca
	v_mov_b32_e32 v108, 0
	s_mov_b32 s26, 0
	v_mov_b64_e32 v[30:31], v[14:15]
	v_mov_b64_e32 v[28:29], v[12:13]
	v_mov_b64_e32 v[26:27], v[10:11]
	v_mov_b64_e32 v[24:25], v[8:9]
	v_mov_b64_e32 v[22:23], v[6:7]
	v_mov_b64_e32 v[20:21], v[4:5]
	v_mov_b64_e32 v[18:19], v[2:3]
	v_mov_b64_e32 v[46:47], v[14:15]
	v_mov_b64_e32 v[44:45], v[12:13]
	v_mov_b64_e32 v[42:43], v[10:11]
	v_mov_b64_e32 v[40:41], v[8:9]
	v_mov_b64_e32 v[38:39], v[6:7]
	v_mov_b64_e32 v[36:37], v[4:5]
	v_mov_b64_e32 v[34:35], v[2:3]
	s_branch .LBB0_772
	.p2align 6

.LBB0_785:
	s_nop 1
	v_max3_f32 v2, v50, v51, v52
	v_max3_f32 v119, v53, v54, v55
	v_max3_f32 v120, v56, v57, v58
	v_max3_f32 v121, v59, v60, v61
	v_max3_f32 v2, v2, v119, v120
	v_max3_f32 v119, v62, v63, v64
	v_max3_f32 v2, v2, v121, v119
	v_max_f32_e32 v2, v2, v65
	v_sub_f32_e32 v119, v2, v113
	v_cmp_ge_f32_e32 vcc, s76, v119
	s_cmp_eq_u64 vcc, exec
	s_cbranch_scc1 .LBB0_787
	v_mov_b32_e32 v119, v2
	s_nop 1
	v_permlane32_swap_b32_e32 v2, v119
	v_max_f32_e32 v2, v2, v119
	v_max_f32_e32 v2, v2, v2
	v_max_f32_e32 v119, v113, v113
	v_max_f32_e32 v119, v119, v2
	v_sub_f32_e32 v2, v113, v119
	v_mul_f32_e32 v2, 0x3fb8aa3b, v2
	v_exp_f32_e32 v2, v2
	v_mov_b32_e32 v113, v119
	v_mul_f32_e32 v108, v108, v2
	v_pk_mul_f32 v[48:49], v[48:49], v[2:3] op_sel_hi:[1,0]
	v_pk_mul_f32 v[46:47], v[46:47], v[2:3] op_sel_hi:[1,0]
	v_pk_mul_f32 v[44:45], v[44:45], v[2:3] op_sel_hi:[1,0]
	v_pk_mul_f32 v[42:43], v[42:43], v[2:3] op_sel_hi:[1,0]
	v_pk_mul_f32 v[40:41], v[40:41], v[2:3] op_sel_hi:[1,0]
	v_pk_mul_f32 v[38:39], v[38:39], v[2:3] op_sel_hi:[1,0]
	v_pk_mul_f32 v[36:37], v[36:37], v[2:3] op_sel_hi:[1,0]
	v_pk_mul_f32 v[34:35], v[34:35], v[2:3] op_sel_hi:[1,0]
	v_pk_mul_f32 v[32:33], v[32:33], v[2:3] op_sel_hi:[1,0]
	v_pk_mul_f32 v[30:31], v[30:31], v[2:3] op_sel_hi:[1,0]
	v_pk_mul_f32 v[28:29], v[28:29], v[2:3] op_sel_hi:[1,0]
	v_pk_mul_f32 v[26:27], v[26:27], v[2:3] op_sel_hi:[1,0]
	v_pk_mul_f32 v[24:25], v[24:25], v[2:3] op_sel_hi:[1,0]
	v_pk_mul_f32 v[22:23], v[22:23], v[2:3] op_sel_hi:[1,0]
	v_pk_mul_f32 v[20:21], v[20:21], v[2:3] op_sel_hi:[1,0]
	v_pk_mul_f32 v[18:19], v[18:19], v[2:3] op_sel_hi:[1,0]
	.p2align 6
